# v3 + P9 attention sink from lane table (v_readlane), keeping the vmcnt(0) before the prefetch loads
# baseline (speedup 1.0000x reference)
.LBB0_869:
	s_ashr_i32 s38, s37, 31
	s_lshr_b32 s2, s38, 25
	s_add_i32 s2, s37, s2
	s_ashr_i32 s39, s2, 7
	s_lshr_b32 s2, s39, 30
	s_add_i32 s2, s39, s2
	s_and_b32 s2, s2, 0x3ffffffc
	s_sub_i32 s2, s39, s2
	s_lshl_b32 s2, s2, 2
	s_or_b32 s8, s2, s22
	s_mul_i32 s2, s34, 0xd000
	s_ashr_i32 s9, s8, 31
	s_add_i32 s36, s2, 0
	s_add_i32 s35, s37, s72
	s_add_i32 s2, s8, 16
	s_nop 3
	v_readlane_b32 s3, v255, s2
	s_nop 1
	v_mov_b32_e32 v156, s3
	s_lshl_b32 s2, s8, 9
	s_add_i32 s2, s2, 0
	v_mov_b32_e32 v157, v123
	s_add_i32 s2, s2, 0x1a000
	v_add3_u32 v113, s36, v140, v144
	v_lshl_add_u32 v74, v157, 2, s2
	ds_read2_b32 v[2:3], v74 offset0:127 offset1:128
	ds_read2_b32 v[4:5], v74 offset0:125 offset1:126
	ds_read2_b32 v[6:7], v74 offset0:119 offset1:120
	ds_read2_b32 v[8:9], v74 offset0:117 offset1:118
	ds_read2_b32 v[10:11], v74 offset0:111 offset1:112
	ds_read2_b32 v[12:13], v74 offset0:109 offset1:110
	ds_read2_b32 v[14:15], v74 offset0:103 offset1:104
	ds_read2_b32 v[20:21], v74 offset0:101 offset1:102
	ds_read_b128 v[16:19], v113
	s_waitcnt lgkmcnt(8)
	v_mov_b32_e32 v0, v3
	v_mov_b32_e32 v1, v2
	s_waitcnt lgkmcnt(7)
	v_mov_b32_e32 v2, v5
	v_mov_b32_e32 v3, v4
	s_waitcnt lgkmcnt(6)
	v_mov_b32_e32 v4, v7
	v_mov_b32_e32 v5, v6
	s_waitcnt lgkmcnt(5)
	v_mov_b32_e32 v6, v9
	v_mov_b32_e32 v7, v8
	s_waitcnt lgkmcnt(4)
	v_mov_b32_e32 v8, v11
	v_mov_b32_e32 v9, v10
	s_waitcnt lgkmcnt(3)
	v_mov_b32_e32 v10, v13
	v_mov_b32_e32 v11, v12
	s_waitcnt lgkmcnt(2)
	v_mov_b32_e32 v12, v15
	v_mov_b32_e32 v13, v14
	s_waitcnt lgkmcnt(1)
	v_mov_b32_e32 v14, v21
	v_mov_b32_e32 v15, v20
	ds_read_b128 v[20:23], v113 offset:32
	v_subrev_u32_e32 v72, 44, v74
	s_waitcnt lgkmcnt(1)
	v_mfma_f32_32x32x16_bf16 v[0:15], v[16:19], v[92:95], v[0:15]
	v_add_u32_e32 v78, 0xffffff9c, v74
	v_add_u32_e32 v135, 0xffffff94, v74
	s_cmpk_lt_i32 s35, 0x1000
	s_cselect_b64 s[12:13], -1, 0
	s_cmpk_gt_i32 s35, 0xfff
	s_cselect_b64 s[10:11], -1, 0
	s_and_b64 vcc, exec, s[10:11]
	s_waitcnt lgkmcnt(0)
	v_mfma_f32_32x32x16_bf16 v[0:15], v[20:23], v[96:99], v[0:15]
	ds_read_b128 v[16:19], v113 offset:64
	ds_read_b128 v[20:23], v113 offset:96
	s_waitcnt lgkmcnt(1)
	v_mfma_f32_32x32x16_bf16 v[0:15], v[16:19], v[100:103], v[0:15]
	s_waitcnt lgkmcnt(0)
	v_mfma_f32_32x32x16_bf16 v[0:15], v[20:23], v[104:107], v[0:15]
	ds_read2_b32 v[18:19], v74 offset0:95 offset1:96
	ds_read2_b32 v[20:21], v74 offset0:93 offset1:94
	ds_read2_b32 v[22:23], v74 offset0:87 offset1:88
	ds_read2_b32 v[24:25], v74 offset0:85 offset1:86
	ds_read2_b32 v[26:27], v74 offset0:79 offset1:80
	ds_read2_b32 v[28:29], v74 offset0:77 offset1:78
	ds_read2_b32 v[30:31], v74 offset0:71 offset1:72
	ds_read2_b32 v[36:37], v74 offset0:69 offset1:70
	ds_read_b128 v[32:35], v113 offset:4608
	s_waitcnt lgkmcnt(8)
	v_mov_b32_e32 v16, v19
	v_mov_b32_e32 v17, v18
	s_waitcnt lgkmcnt(7)
	v_mov_b32_e32 v18, v21
	v_mov_b32_e32 v19, v20
	s_waitcnt lgkmcnt(6)
	v_mov_b32_e32 v20, v23
	v_mov_b32_e32 v21, v22
	s_waitcnt lgkmcnt(5)
	v_mov_b32_e32 v22, v25
	v_mov_b32_e32 v23, v24
	s_waitcnt lgkmcnt(4)
	v_mov_b32_e32 v24, v27
	v_mov_b32_e32 v25, v26
	s_waitcnt lgkmcnt(3)
	v_mov_b32_e32 v26, v29
	v_mov_b32_e32 v27, v28
	s_waitcnt lgkmcnt(2)
	v_mov_b32_e32 v28, v31
	v_mov_b32_e32 v29, v30
	s_waitcnt lgkmcnt(1)
	v_mov_b32_e32 v30, v37
	v_mov_b32_e32 v31, v36
	ds_read_b128 v[36:39], v113 offset:4640
	s_waitcnt lgkmcnt(1)
	v_mfma_f32_32x32x16_bf16 v[16:31], v[32:35], v[92:95], v[16:31]
	s_waitcnt lgkmcnt(0)
	v_mfma_f32_32x32x16_bf16 v[16:31], v[36:39], v[96:99], v[16:31]
	ds_read_b128 v[32:35], v113 offset:4672
	ds_read_b128 v[36:39], v113 offset:4704
	s_waitcnt lgkmcnt(1)
	v_mfma_f32_32x32x16_bf16 v[16:31], v[32:35], v[100:103], v[16:31]
	s_waitcnt lgkmcnt(0)
	v_mfma_f32_32x32x16_bf16 v[16:31], v[36:39], v[104:107], v[16:31]
	ds_read2_b32 v[34:35], v74 offset0:63 offset1:64
	ds_read2_b32 v[36:37], v74 offset0:61 offset1:62
	ds_read2_b32 v[38:39], v74 offset0:55 offset1:56
	ds_read2_b32 v[40:41], v74 offset0:53 offset1:54
	ds_read2_b32 v[42:43], v74 offset0:47 offset1:48
	ds_read2_b32 v[44:45], v74 offset0:45 offset1:46
	ds_read2_b32 v[46:47], v74 offset0:39 offset1:40
	ds_read2_b32 v[52:53], v74 offset0:37 offset1:38
	ds_read_b128 v[48:51], v113 offset:9216
	s_waitcnt lgkmcnt(8)
	v_mov_b32_e32 v32, v35
	v_mov_b32_e32 v33, v34
	s_waitcnt lgkmcnt(7)
	v_mov_b32_e32 v34, v37
	v_mov_b32_e32 v35, v36
	s_waitcnt lgkmcnt(6)
	v_mov_b32_e32 v36, v39
	v_mov_b32_e32 v37, v38
	s_waitcnt lgkmcnt(5)
	v_mov_b32_e32 v38, v41
	v_mov_b32_e32 v39, v40
	s_waitcnt lgkmcnt(4)
	v_mov_b32_e32 v40, v43
	v_mov_b32_e32 v41, v42
	s_waitcnt lgkmcnt(3)
	v_mov_b32_e32 v42, v45
	v_mov_b32_e32 v43, v44
	s_waitcnt lgkmcnt(2)
	v_mov_b32_e32 v44, v47
	v_mov_b32_e32 v45, v46
	s_waitcnt lgkmcnt(1)
	v_mov_b32_e32 v46, v53
	v_mov_b32_e32 v47, v52
	ds_read_b128 v[52:55], v113 offset:9248
	s_waitcnt lgkmcnt(1)
	v_mfma_f32_32x32x16_bf16 v[32:47], v[48:51], v[92:95], v[32:47]
	s_waitcnt lgkmcnt(0)
	v_mfma_f32_32x32x16_bf16 v[32:47], v[52:55], v[96:99], v[32:47]
	ds_read_b128 v[48:51], v113 offset:9280
	ds_read_b128 v[52:55], v113 offset:9312
	s_waitcnt lgkmcnt(1)
	v_mfma_f32_32x32x16_bf16 v[32:47], v[48:51], v[100:103], v[32:47]
	s_waitcnt lgkmcnt(0)
	v_mfma_f32_32x32x16_bf16 v[32:47], v[52:55], v[104:107], v[32:47]
	ds_read2_b32 v[50:51], v74 offset0:31 offset1:32
	ds_read2_b32 v[52:53], v74 offset0:29 offset1:30
	ds_read2_b32 v[54:55], v74 offset0:23 offset1:24
	ds_read2_b32 v[56:57], v74 offset0:21 offset1:22
	ds_read2_b32 v[58:59], v74 offset0:15 offset1:16
	ds_read2_b32 v[60:61], v74 offset0:13 offset1:14
	ds_read2_b32 v[62:63], v74 offset0:7 offset1:8
	ds_read2_b32 v[68:69], v74 offset0:5 offset1:6
	ds_read_b128 v[64:67], v113 offset:13824
	s_waitcnt lgkmcnt(8)
	v_mov_b32_e32 v48, v51
	v_mov_b32_e32 v49, v50
	s_waitcnt lgkmcnt(7)
	v_mov_b32_e32 v50, v53
	v_mov_b32_e32 v51, v52
	s_waitcnt lgkmcnt(6)
	v_mov_b32_e32 v52, v55
	v_mov_b32_e32 v53, v54
	s_waitcnt lgkmcnt(5)
	v_mov_b32_e32 v54, v57
	v_mov_b32_e32 v55, v56
	s_waitcnt lgkmcnt(4)
	v_mov_b32_e32 v56, v59
	v_mov_b32_e32 v57, v58
	s_waitcnt lgkmcnt(3)
	v_mov_b32_e32 v58, v61
	v_mov_b32_e32 v59, v60
	s_waitcnt lgkmcnt(2)
	v_mov_b32_e32 v60, v63
	v_mov_b32_e32 v61, v62
	s_waitcnt lgkmcnt(1)
	v_mov_b32_e32 v62, v69
	v_mov_b32_e32 v63, v68
	ds_read_b128 v[68:71], v113 offset:13856
	s_waitcnt lgkmcnt(1)
	v_mfma_f32_32x32x16_bf16 v[48:63], v[64:67], v[92:95], v[48:63]
	s_waitcnt lgkmcnt(0)
	v_mfma_f32_32x32x16_bf16 v[48:63], v[68:71], v[96:99], v[48:63]
	ds_read_b128 v[64:67], v113 offset:13888
	ds_read_b128 v[68:71], v113 offset:13920
	s_waitcnt lgkmcnt(1)
	v_mfma_f32_32x32x16_bf16 v[48:63], v[64:67], v[100:103], v[48:63]
	v_add_u32_e32 v64, -4, v74
	v_add_u32_e32 v65, -12, v74
	s_waitcnt lgkmcnt(0)
	v_mfma_f32_32x32x16_bf16 v[48:63], v[68:71], v[104:107], v[48:63]
	v_subrev_u32_e32 v70, 36, v74
	ds_read2_b32 v[66:67], v64 offset1:1
	ds_read2_b32 v[68:69], v65 offset1:1
	ds_read2_b32 v[70:71], v70 offset1:1
	ds_read2_b32 v[72:73], v72 offset1:1
	v_add_u32_e32 v64, 0xffffffbc, v74
	v_add_u32_e32 v65, 0xffffffb4, v74
	ds_read2_b32 v[74:75], v64 offset1:1
	ds_read2_b32 v[76:77], v65 offset1:1
	ds_read2_b32 v[78:79], v78 offset1:1
	ds_read2_b32 v[138:139], v135 offset1:1
	ds_read_b128 v[158:161], v113 offset:18432
	ds_read_b128 v[162:165], v113 offset:18464
	s_waitcnt lgkmcnt(9)
	v_mov_b32_e32 v64, v67
	v_mov_b32_e32 v65, v66
	s_waitcnt lgkmcnt(8)
	v_mov_b32_e32 v66, v69
	v_mov_b32_e32 v67, v68
	s_waitcnt lgkmcnt(7)
	v_mov_b32_e32 v68, v71
	v_mov_b32_e32 v69, v70
	s_waitcnt lgkmcnt(6)
	v_mov_b32_e32 v70, v73
	v_mov_b32_e32 v71, v72
	s_waitcnt lgkmcnt(5)
	v_mov_b32_e32 v72, v75
	v_mov_b32_e32 v73, v74
	s_waitcnt lgkmcnt(4)
	v_mov_b32_e32 v74, v77
	v_mov_b32_e32 v75, v76
	s_waitcnt lgkmcnt(3)
	v_mov_b32_e32 v76, v79
	v_mov_b32_e32 v77, v78
	s_waitcnt lgkmcnt(2)
	v_mov_b32_e32 v78, v139
	v_mov_b32_e32 v79, v138
	s_waitcnt lgkmcnt(1)
	s_nop 0
	v_mfma_f32_32x32x16_bf16 v[64:79], v[158:161], v[92:95], v[64:79]
	s_waitcnt lgkmcnt(0)
	v_mfma_f32_32x32x16_bf16 v[64:79], v[162:165], v[96:99], v[64:79]
	ds_read_b128 v[158:161], v113 offset:18496
	ds_read_b128 v[162:165], v113 offset:18528
	s_waitcnt lgkmcnt(1)
	v_mfma_f32_32x32x16_bf16 v[64:79], v[158:161], v[100:103], v[64:79]
	s_waitcnt lgkmcnt(0)
	v_mfma_f32_32x32x16_bf16 v[64:79], v[162:165], v[104:107], v[64:79]
	s_waitcnt vmcnt(0)
	s_cbranch_vccnz .LBB0_885
	s_ashr_i32 s2, s35, 31
	s_lshr_b32 s3, s2, 23
	s_lshr_b32 s2, s2, 25
	s_add_i32 s2, s35, s2
	s_ashr_i32 s6, s2, 7
	s_add_i32 s3, s35, s3
	s_lshr_b32 s2, s6, 30
	s_ashr_i32 s14, s3, 9
	s_add_i32 s2, s6, s2
	s_lshl_b32 s9, s6, 13
	s_add_i32 s17, s23, s30
	s_and_b32 s2, s2, -4
	s_ashr_i32 s15, s14, 31
	s_sub_i32 s17, s17, s9
	s_sub_i32 s16, s6, s2
	s_lshl_b64 s[2:3], s[14:15], 13
	s_ashr_i32 s40, s17, 31
	s_add_u32 s2, s2, s17
	s_addc_u32 s3, s3, s40
	v_mov_b32_e32 v81, s3
	v_or_b32_e32 v80, s2, v122
	s_lshl_b32 s2, s16, 8
	v_lshlrev_b64 v[80:81], 11, v[80:81]
	s_or_b32 s2, s2, s26
	v_lshl_add_u64 v[80:81], s[4:5], 0, v[80:81]
	s_ashr_i32 s3, s2, 31
	v_lshl_add_u64 v[80:81], s[2:3], 1, v[80:81]
	v_mov_b32_e32 v135, v112
	v_lshl_add_u64 v[80:81], v[80:81], 0, v[134:135]
	global_load_dwordx4 v[92:95], v[80:81], off
	global_load_dwordx4 v[96:99], v[80:81], off offset:32
	global_load_dwordx4 v[100:103], v[80:81], off offset:64
	global_load_dwordx4 v[104:107], v[80:81], off offset:96
	s_lshl_b64 s[2:3], s[14:15], 22
	s_add_u32 s40, s18, s2
	s_addc_u32 s41, s19, s3
	s_lshl_b32 s16, s16, 6
	s_ashr_i32 s17, s16, 31
	s_lshl_b64 s[2:3], s[16:17], 1
	s_add_u32 s2, s40, s2
	s_addc_u32 s3, s41, s3
	v_mov_b32_e32 v137, v112
	v_lshl_add_u64 v[118:119], s[2:3], 0, v[136:137]
	s_sub_i32 s2, s30, s9
	v_mov_b32_e32 v113, v112
	v_add_u32_e32 v84, s2, v152
	v_mov_b32_e32 v114, v112
	v_mov_b32_e32 v115, v112
	v_mov_b64_e32 v[80:81], v[112:113]
	v_cmp_lt_i32_e32 vcc, -1, v84
	v_mov_b64_e32 v[82:83], v[114:115]
	s_and_saveexec_b64 s[2:3], vcc
	s_cbranch_execz .LBB0_872
	v_mov_b32_e32 v85, v112
	v_lshlrev_b64 v[80:81], 9, v[84:85]
	v_lshl_add_u64 v[80:81], v[118:119], 0, v[80:81]
	global_load_dwordx4 v[80:83], v[80:81], off
